# static priority raise given to the older half (waves 0-3) of the attention loop instead of the younger half (A/B of halves)
# speedup vs baseline: 1.0048x; 1.0048x over previous
.LBB0_1251:
	s_waitcnt vmcnt(0) lgkmcnt(0)
	s_barrier
	v_lshl_add_u64 v[36:37], v[230:231], 0, s[20:21]
	s_mov_b32 s4, m0
	s_mov_b32 m0, s71
	s_nop 0
	global_load_lds_dwordx4 v[36:37], off
	s_mov_b32 m0, s4
	s_cmp_lg_u32 0, -1
	s_cselect_b32 s4, 0, 0
	s_add_i32 s4, s4, s69
	v_lshl_add_u64 v[36:37], v[232:233], 0, s[16:17]
	s_add_i32 s5, s4, 0xa000
	s_mov_b32 s36, m0
	s_mov_b32 m0, s5
	s_nop 0
	global_load_lds_dwordx4 v[36:37], off
	s_mov_b32 m0, s36
	v_lshl_add_u64 v[36:37], v[232:233], 0, s[22:23]
	s_add_i32 s4, s4, 0xc000
	s_mov_b32 s5, m0
	s_mov_b32 m0, s4
	s_nop 0
	global_load_lds_dwordx4 v[36:37], off
	s_mov_b32 m0, s5
	ds_read_b128 v[206:209], v252 offset:8192
	ds_read_b128 v[202:205], v252 offset:8704
	ds_read_b128 v[198:201], v252 offset:10240
	ds_read_b128 v[194:197], v252 offset:10752
	ds_read_b128 v[190:193], v252 offset:12288
	ds_read_b128 v[186:189], v252 offset:12800
	ds_read_b128 v[182:185], v252 offset:14336
	ds_read_b128 v[178:181], v252 offset:14848
	s_waitcnt vmcnt(3) lgkmcnt(0)
	s_barrier
	s_cmp_ge_i32 s37, 4
	s_cbranch_scc1 .LBB0_1253
	s_setprio 1
